# weight conversion shares: 512 more tiles converted ahead by the out-GEMM filler, phase-1 loop has at most 7 tiles per wave
# baseline (speedup 1.0000x reference)
.LBB0_78:
	s_or_b64 exec, exec, s[0:1]
	v_readlane_b32 s0, v255, 6
	v_readlane_b32 s1, v255, 7
	s_mov_b32 s21, s1
	v_readlane_b32 s0, v251, 1
	s_lshl_b64 s[16:17], s[20:21], 12
	v_readlane_b32 s8, v251, 9
	v_readlane_b32 s10, v251, 11
	v_readlane_b32 s11, v251, 12
	v_readlane_b32 s12, v251, 13
	v_readlane_b32 s9, v251, 10
	v_readlane_b32 s13, v251, 14
	s_add_u32 s8, s12, s16
	v_sub_co_u32_e64 v2, s[10:11], s20, 1
	v_writelane_b32 v255, s16, 28
	s_addc_u32 s9, s13, s17
	s_xor_b64 s[12:13], s[10:11], -1
	v_readlane_b32 s1, v251, 2
	v_readlane_b32 s14, v251, 15
	v_readlane_b32 s15, v251, 16
	s_cmp_lg_u32 s20, 0
	s_cselect_b64 s[14:15], -1, 0
	s_and_b64 s[0:1], s[10:11], exec
	v_readlane_b32 s2, v251, 3
	s_cselect_b32 s0, 0, 0x3200
	v_writelane_b32 v255, s17, 29
	s_add_i32 s2, s0, s89
	s_lshl_b64 s[16:17], s[20:21], 27
	s_lshl_b64 s[0:1], s[20:21], 22
	v_readlane_b32 s3, v251, 4
	s_add_u32 s18, s68, s16
	s_addc_u32 s19, s69, s17
	v_readlane_b32 s3, v251, 57
	s_add_u32 s78, s3, s26
	v_readlane_b32 s3, v251, 58
	v_readlane_b32 s4, v251, 5
	s_addc_u32 s79, s3, 0
	v_readlane_b32 s3, v251, 59
	v_readlane_b32 s5, v251, 6
	s_add_u32 s4, s3, s26
	v_readlane_b32 s3, v251, 60
	s_addc_u32 s5, s3, 0
	v_readlane_b32 s36, v251, 35
	v_writelane_b32 v255, s4, 30
	v_readlane_b32 s48, v251, 47
	v_readlane_b32 s49, v251, 48
	v_writelane_b32 v255, s5, 31
	s_mov_b64 s[4:5], s[20:21]
	s_add_u32 s20, s48, s0
	v_mov_b32_e32 v3, v0
	s_addc_u32 s21, s49, s1
	v_readlane_b32 s0, v251, 61
	v_ashrrev_i32_e32 v4, 6, v3
	v_add_u32_e32 v117, s2, v4
	s_add_u32 s2, s0, s26
	v_readlane_b32 s0, v251, 62
	s_addc_u32 s3, s0, 0
	v_readlane_b32 s0, v251, 63
	v_readlane_b32 s37, v251, 36
	v_readlane_b32 s38, v251, 37
	v_readlane_b32 s39, v251, 38
	v_readlane_b32 s40, v251, 39
	v_readlane_b32 s41, v251, 40
	v_readlane_b32 s42, v251, 41
	v_readlane_b32 s43, v251, 42
	v_readlane_b32 s44, v251, 43
	v_readlane_b32 s45, v251, 44
	v_readlane_b32 s46, v251, 45
	v_readlane_b32 s47, v251, 46
	v_readlane_b32 s50, v251, 49
	v_readlane_b32 s51, v251, 50
	s_add_u32 s34, s0, s26
	v_readlane_b32 s0, v252, 0
	s_addc_u32 s35, s0, 0
	s_mul_i32 s1, s4, 0x1b10000
	v_readlane_b32 s36, v251, 19
	s_mul_hi_u32 s0, s4, 0x1b10000
	v_readlane_b32 s37, v251, 20
	s_add_u32 s22, s36, s1
	v_readlane_b32 s38, v251, 21
	v_readlane_b32 s39, v251, 22
	s_addc_u32 s23, s37, s0
	s_movk_i32 s0, 0x4100
	v_lshlrev_b32_e32 v5, 2, v3
	s_mul_hi_u32 s39, s4, 9
	s_mul_i32 s38, s4, 9
	v_mul_hi_u32 v115, v2, 9
	v_mul_lo_u32 v114, v2, 9
	v_mul_lo_u32 v2, v4, s0
	v_bfe_u32 v123, v3, 4, 2
	v_and_b32_e32 v162, 60, v5
	v_bfe_u32 v164, v3, 3, 3
	v_lshlrev_b32_e32 v3, 3, v3
	s_mul_hi_u32 s25, s4, 3
	v_writelane_b32 v255, s4, 32
	v_add_u32_e32 v2, 0, v2
	v_lshlrev_b32_e32 v5, 2, v162
	v_mul_u32_u24_e32 v6, 0x104, v123
	v_and_b32_e32 v116, 56, v3
	v_writelane_b32 v255, s5, 33
	v_readlane_b32 s0, v252, 1
	v_add3_u32 v163, v2, v5, v6
	v_mul_u32_u24_e32 v3, 0x104, v116
	v_lshlrev_b32_e32 v5, 2, v164
	v_writelane_b32 v255, s2, 34
	s_add_u32 s30, s0, s26
	v_readlane_b32 s0, v252, 2
	v_add3_u32 v165, v2, v3, v5
	v_lshlrev_b32_e32 v130, 1, v116
	v_writelane_b32 v255, s3, 35
	s_addc_u32 s31, s0, 0
	v_mov_b32_e32 v2, 0xffff6d60
	s_movk_i32 s0, 0x6950
	s_mul_i32 s24, s4, 3
	v_lshl_add_u64 v[118:119], s[2:3], 0, v[130:131]
	v_writelane_b32 v255, s26, 36
	v_lshl_add_u64 v[120:121], s[30:31], 0, v[130:131]
	v_mul_u32_u24_e32 v122, 0x1b10, v123
	v_lshl_add_u32 v166, v117, 1, v2
	v_lshl_add_u32 v167, v117, 14, v241
	v_lshl_add_u32 v168, v117, 3, v250
	v_cmp_gt_i32_e64 s[2:3], s0, v117
	v_cmp_gt_i32_e64 s[26:27], 4, v4
	v_cmp_lt_i32_e64 s[0:1], 3, v4
	s_mov_b64 s[28:29], -1
	v_readlane_b32 s6, v251, 7
	v_readlane_b32 s7, v251, 8
	v_readlane_b32 s40, v251, 23
	v_readlane_b32 s41, v251, 24
	v_readlane_b32 s42, v251, 25
	v_readlane_b32 s43, v251, 26
	v_readlane_b32 s44, v251, 27
	v_readlane_b32 s45, v251, 28
	v_readlane_b32 s46, v251, 29
	v_readlane_b32 s47, v251, 30
	v_readlane_b32 s48, v251, 31
	v_readlane_b32 s49, v251, 32
	v_readlane_b32 s50, v251, 33
	v_readlane_b32 s51, v251, 34
	s_branch .LBB0_80

.LBB0_1018:
	s_or_b64 exec, exec, s[18:19]
	s_movk_i32 s0, 0x2fff
	v_add_u32_e32 v10, 0x200, v3
	v_cmp_lt_i32_e32 vcc, s0, v3
	v_add_u32_e32 v8, 0xd880000, v8
	v_add_u32_e32 v52, 0x8000, v52
	v_add_u32_e32 v53, 0x800, v53
	v_add_u32_e32 v54, 0x800000, v54
	v_add_u32_e32 v55, 0x1000, v55
	s_or_b64 s[16:17], vcc, s[16:17]
	v_mov_b32_e32 v3, v10
	s_andn2_b64 exec, exec, s[16:17]
	s_cbranch_execz .LBB0_1046
